# P0 rmsnorm: the eight 1-KB loads of each input row marked non-temporal (x is streamed once here)
# speedup vs baseline: 1.0118x; 1.0118x over previous
; __device__ __forceinline__ unsigned cvt_pk_bf16(float lo, float hi) { unsigned r; asm volatile("v_cvt_pk_bf16_f32 %0, %1, %2" : "=v"(r) : "v"(lo), "v"(hi)); return r; }
; __device__ __forceinline__ unsigned cvt_pk4_fp8(float a, float b, float c, float d) { int w; asm("" : "=v"(w));     w = __builtin_amdgcn_cvt_pk_fp8_f32(a, b, w, false); w = __builtin_amdgcn_cvt_pk_fp8_f32(c, d, w, true); return (unsigned)w; }
; __global__ void __launch_bounds__(512, 2) fwd_kernel(Params p) {
;     ...
;         for (int m = gw; m < T; m += NGW) {
;             const f32x4* xr = (const f32x4*)(p.in[I_X] + (size_t)m * DM) + lane; const f32x4* gr = (const f32x4*)p.in[I_GMIX] + lane;
;             f32x4 v[8]; float s = 0.f;
; #pragma unroll
;             for (int j = 0; j < 8; ++j) { v[j] = xr[64 * j]; s += (v[j].x * v[j].x + v[j].y * v[j].y) + (v[j].z * v[j].z + v[j].w * v[j].w); }
;             const float rstd = rsqrtf(wave_sum(s) * (1.f / DM) + RMS_EPS);
;             u32x2* o8 = (u32x2*)(Hb + (size_t)m * DM) + lane; unsigned* o4 = (unsigned*)(H8 + (size_t)m * DM) + lane;
; #pragma unroll
;             for (int j = 0; j < 8; ++j) { const f32x4 g = gr[64 * j]; const f32x4 hv = v[j] * rstd * g; u32x2 w; w.x = cvt_pk_bf16(hv.x, hv.y); w.y = cvt_pk_bf16(hv.z, hv.w); o8[64 * j] = w; o4[64 * j] = cvt_pk4_fp8(hv.x, hv.y, hv.z, hv.w); }
;         }
.LBB0_46:
	v_add_co_u32_e32 v60, vcc, 0xfffff000, v30
	global_load_dwordx4 v[12:15], v[30:31], off offset:-3072 nt
	global_load_dwordx4 v[8:11], v[30:31], off offset:-2048 nt
	global_load_dwordx4 v[4:7], v[30:31], off offset:-1024 nt
	v_addc_co_u32_e32 v61, vcc, -1, v31, vcc
	global_load_dwordx4 v[40:43], v[60:61], off offset:-3072 nt
	global_load_dwordx4 v[44:47], v[60:61], off offset:-2048 nt
	global_load_dwordx4 v[48:51], v[60:61], off offset:-1024 nt
	global_load_dwordx4 v[52:55], v[30:31], off offset:-4096 nt
	global_load_dwordx4 v[0:3], v[30:31], off nt
	global_load_dwordx4 v[56:59], v[16:17], off
	s_add_i32 s12, s12, s18
	s_cmpk_gt_i32 s12, 0x3fff
	v_lshl_add_u64 v[30:31], v[30:31], 0, s[10:11]
	s_waitcnt vmcnt(5)
	v_mov_b32_e32 v70, v41
	v_pk_mul_f32 v[60:61], v[10:11], v[10:11]
	v_pk_mul_f32 v[62:63], v[8:9], v[8:9]
	v_mul_f32_e32 v64, v5, v5
	v_mul_f32_e32 v66, v7, v7
	s_waitcnt vmcnt(1)
	v_mul_f32_e32 v81, v2, v2
	v_mul_f32_e32 v88, v3, v3
	v_pk_mov_b32 v[68:69], v[62:63], v[60:61] op_sel:[1,0]
	v_mov_b32_e32 v63, v61
	v_pk_fma_f32 v[60:61], v[4:5], v[4:5], v[64:65] op_sel_hi:[1,1,0]
	v_pk_fma_f32 v[64:65], v[6:7], v[6:7], v[66:67] op_sel_hi:[1,1,0]
	v_mov_b32_e32 v71, v45
	v_mov_b32_e32 v74, v43
	v_mov_b32_e32 v75, v47
	v_mov_b32_e32 v66, v40
	v_mov_b32_e32 v67, v44
	v_mov_b32_e32 v72, v42
	v_mov_b32_e32 v73, v46
	v_pk_mul_f32 v[76:77], v[50:51], v[50:51]
	v_pk_mul_f32 v[78:79], v[48:49], v[48:49]
	v_pk_add_f32 v[62:63], v[68:69], v[62:63]
	v_mov_b32_e32 v61, v81
	v_mov_b32_e32 v65, v88
	v_pk_mul_f32 v[68:69], v[70:71], v[70:71]
	v_pk_mul_f32 v[70:71], v[74:75], v[74:75]
	v_pk_mov_b32 v[74:75], v[78:79], v[76:77] op_sel:[1,0]
	v_mov_b32_e32 v79, v77
	v_pk_add_f32 v[60:61], v[60:61], v[64:65]
	v_pk_fma_f32 v[64:65], v[66:67], v[66:67], v[68:69]
	v_pk_fma_f32 v[66:67], v[72:73], v[72:73], v[70:71]
	v_mul_f32_e32 v83, v13, v13
	v_mul_f32_e32 v80, v53, v53
	v_mul_f32_e32 v82, v55, v55
	v_pk_add_f32 v[68:69], v[74:75], v[78:79]
	v_pk_add_f32 v[64:65], v[64:65], v[66:67]
	v_mul_f32_e32 v39, v12, v12
	v_mul_f32_e32 v84, v14, v14
	v_mul_f32_e32 v85, v15, v15
	v_pk_fma_f32 v[76:77], v[52:53], v[52:53], v[80:81] op_sel_hi:[1,1,0]
	v_pk_fma_f32 v[80:81], v[54:55], v[54:55], v[82:83] op_sel_hi:[1,1,0]
	v_pk_add_f32 v[66:67], v[68:69], v[68:69] op_sel:[0,1] op_sel_hi:[1,0]
	v_pk_add_f32 v[64:65], v[64:65], v[64:65] op_sel:[0,1] op_sel_hi:[1,0]
	v_mov_b32_e32 v77, v84
	v_mov_b32_e32 v81, v85
	v_mov_b32_e32 v67, v83
	v_mov_b32_e32 v65, v39
	v_pk_add_f32 v[68:69], v[76:77], v[80:81]
	v_pk_add_f32 v[64:65], v[64:65], v[66:67]
	v_mul_f32_e32 v86, v0, v0
	v_pk_add_f32 v[64:65], v[64:65], v[68:69]
	v_mul_f32_e32 v87, v1, v1
	v_pk_add_f32 v[62:63], v[62:63], v[62:63] op_sel:[0,1] op_sel_hi:[1,0]
	v_pk_add_f32 v[64:65], v[64:65], v[64:65] op_sel:[0,1] op_sel_hi:[1,0]
	v_mov_b32_e32 v63, v87
	v_mov_b32_e32 v65, v86
	v_pk_add_f32 v[62:63], v[64:65], v[62:63]
	s_nop 0
	v_pk_add_f32 v[60:61], v[62:63], v[60:61]
	v_add_f32_e32 v39, v60, v61
	ds_bpermute_b32 v60, v32, v39
	s_waitcnt lgkmcnt(0)
	v_add_f32_e32 v39, v39, v60
	ds_bpermute_b32 v60, v33, v39
	s_waitcnt lgkmcnt(0)
	v_add_f32_e32 v39, v39, v60
	ds_bpermute_b32 v62, v34, v39
	v_lshl_add_u64 v[60:61], s[28:29], 0, v[20:21]
	v_add_co_u32_e32 v60, vcc, s1, v60
	v_lshl_add_u64 v[20:21], v[20:21], 0, s[8:9]
	s_waitcnt lgkmcnt(0)
	v_add_f32_e32 v39, v39, v62
	ds_bpermute_b32 v64, v35, v39
	v_addc_co_u32_e32 v61, vcc, 0, v61, vcc
	v_lshl_add_u64 v[62:63], s[28:29], 0, v[28:29]
	v_add_co_u32_e64 v62, s[4:5], s3, v62
	s_waitcnt lgkmcnt(0)
	v_add_f32_e32 v39, v39, v64
	ds_bpermute_b32 v64, v36, v39
	v_lshl_add_u64 v[28:29], v[28:29], 0, s[6:7]
	s_waitcnt lgkmcnt(0)
	v_add_f32_e32 v39, v39, v64
	ds_bpermute_b32 v64, v37, v39
	s_waitcnt lgkmcnt(0)
	v_add_f32_e32 v39, v39, v64
	v_fmamk_f32 v39, v39, 0x3a000000, v38
	v_mul_f32_e32 v64, 0x4b800000, v39
	v_cmp_gt_f32_e32 vcc, s0, v39
	s_nop 1
	v_cndmask_b32_e32 v39, v39, v64, vcc
	v_rsq_f32_e32 v39, v39
	s_nop 0
	v_mul_f32_e32 v64, 0x45800000, v39
	v_cndmask_b32_e32 v64, v39, v64, vcc
	v_pk_mul_f32 v[40:41], v[64:65], v[40:41] op_sel_hi:[0,1]
	s_waitcnt vmcnt(0)
; __device__ __forceinline__ unsigned cvt_pk_bf16(float lo, float hi) { unsigned r; asm volatile("v_cvt_pk_bf16_f32 %0, %1, %2" : "=v"(r) : "v"(lo), "v"(hi)); return r; }
; __device__ __forceinline__ unsigned cvt_pk4_fp8(float a, float b, float c, float d) { int w; asm("" : "=v"(w));     w = __builtin_amdgcn_cvt_pk_fp8_f32(a, b, w, false); w = __builtin_amdgcn_cvt_pk_fp8_f32(c, d, w, true); return (unsigned)w; }
; __global__ void __launch_bounds__(512, 2) fwd_kernel(Params p) {
;     ...
; #pragma unroll
;             for (int j = 0; j < 8; ++j) { const f32x4 g = gr[64 * j]; const f32x4 hv = v[j] * rstd * g; u32x2 w; w.x = cvt_pk_bf16(hv.x, hv.y); w.y = cvt_pk_bf16(hv.z, hv.w); o8[64 * j] = w; o4[64 * j] = cvt_pk4_fp8(hv.x, hv.y, hv.z, hv.w); }
	v_pk_mul_f32 v[40:41], v[56:57], v[40:41]
	v_pk_mul_f32 v[42:43], v[64:65], v[42:43] op_sel_hi:[0,1]
	v_cvt_pk_fp8_f32 v66, v40, v41
	v_pk_mul_f32 v[42:43], v[58:59], v[42:43]
	v_cvt_pk_bf16_f32 v40, v40, v41
	v_addc_co_u32_e64 v63, vcc, 0, v63, s[4:5]
	v_cvt_pk_fp8_f32 v66, v42, v43 op_sel:[0,0,1]
	v_cvt_pk_bf16_f32 v41, v42, v43
	global_store_dwordx2 v[60:61], v[40:41], off
	global_store_dword v[62:63], v66, off
	global_load_dwordx4 v[40:43], v[16:17], off offset:1024
	v_pk_mul_f32 v[44:45], v[64:65], v[44:45] op_sel_hi:[0,1]
	v_pk_mul_f32 v[12:13], v[64:65], v[12:13] op_sel_hi:[0,1]
	v_pk_mul_f32 v[14:15], v[64:65], v[14:15] op_sel_hi:[0,1]
	v_pk_mul_f32 v[8:9], v[64:65], v[8:9] op_sel_hi:[0,1]
	v_pk_mul_f32 v[10:11], v[64:65], v[10:11] op_sel_hi:[0,1]
	v_pk_mul_f32 v[4:5], v[64:65], v[4:5] op_sel_hi:[0,1]
	v_pk_mul_f32 v[6:7], v[64:65], v[6:7] op_sel_hi:[0,1]
	v_pk_mul_f32 v[0:1], v[64:65], v[0:1] op_sel_hi:[0,1]
	s_waitcnt vmcnt(0)
	v_pk_mul_f32 v[40:41], v[40:41], v[44:45]
	s_nop 0
	v_cvt_pk_fp8_f32 v39, v40, v41
	v_pk_mul_f32 v[44:45], v[64:65], v[46:47] op_sel_hi:[0,1]
	v_pk_mul_f32 v[42:43], v[42:43], v[44:45]
	v_cvt_pk_bf16_f32 v40, v40, v41
	v_pk_mul_f32 v[44:45], v[64:65], v[48:49] op_sel_hi:[0,1]
	v_cvt_pk_fp8_f32 v39, v42, v43 op_sel:[0,0,1]
	v_cvt_pk_bf16_f32 v41, v42, v43
	global_store_dwordx2 v[60:61], v[40:41], off offset:512
	global_store_dword v[62:63], v39, off offset:256
	global_load_dwordx4 v[40:43], v[16:17], off offset:2048
	s_waitcnt vmcnt(0)
	v_pk_mul_f32 v[40:41], v[40:41], v[44:45]
	s_nop 0
	v_cvt_pk_fp8_f32 v39, v40, v41
	v_pk_mul_f32 v[44:45], v[64:65], v[50:51] op_sel_hi:[0,1]
	v_pk_mul_f32 v[42:43], v[42:43], v[44:45]
	v_cvt_pk_bf16_f32 v40, v40, v41
	v_pk_mul_f32 v[44:45], v[64:65], v[52:53] op_sel_hi:[0,1]
	v_cvt_pk_fp8_f32 v39, v42, v43 op_sel:[0,0,1]
	v_cvt_pk_bf16_f32 v41, v42, v43
	global_store_dwordx2 v[60:61], v[40:41], off offset:1024
	global_store_dword v[62:63], v39, off offset:512
	global_load_dwordx4 v[40:43], v[16:17], off offset:3072
	s_waitcnt vmcnt(0)
	v_pk_mul_f32 v[40:41], v[40:41], v[44:45]
	s_nop 0
	v_cvt_pk_fp8_f32 v39, v40, v41
	v_pk_mul_f32 v[44:45], v[64:65], v[54:55] op_sel_hi:[0,1]
	v_pk_mul_f32 v[42:43], v[42:43], v[44:45]
	v_cvt_pk_bf16_f32 v40, v40, v41
	s_nop 0
	v_cvt_pk_fp8_f32 v39, v42, v43 op_sel:[0,0,1]
	v_cvt_pk_bf16_f32 v41, v42, v43
	global_store_dwordx2 v[60:61], v[40:41], off offset:1536
	global_store_dword v[62:63], v39, off offset:768
	global_load_dwordx4 v[40:43], v[18:19], off
	s_waitcnt vmcnt(0)
	v_pk_mul_f32 v[12:13], v[40:41], v[12:13]
	s_nop 0
	v_cvt_pk_fp8_f32 v39, v12, v13
	v_pk_mul_f32 v[14:15], v[42:43], v[14:15]
	v_cvt_pk_bf16_f32 v12, v12, v13
	s_nop 0
	v_cvt_pk_fp8_f32 v39, v14, v15 op_sel:[0,0,1]
	v_cvt_pk_bf16_f32 v13, v14, v15
	global_store_dwordx2 v[60:61], v[12:13], off offset:2048
	global_store_dword v[62:63], v39, off offset:1024
	global_load_dwordx4 v[12:15], v[22:23], off
	s_waitcnt vmcnt(0)
	v_pk_mul_f32 v[8:9], v[12:13], v[8:9]
	s_nop 0
	v_cvt_pk_fp8_f32 v39, v8, v9
	v_pk_mul_f32 v[10:11], v[14:15], v[10:11]
	v_cvt_pk_bf16_f32 v8, v8, v9
	v_cvt_pk_fp8_f32 v39, v10, v11 op_sel:[0,0,1]
	v_cvt_pk_bf16_f32 v9, v10, v11
	global_store_dwordx2 v[60:61], v[8:9], off offset:2560
	global_store_dword v[62:63], v39, off offset:1280
	global_load_dwordx4 v[8:11], v[24:25], off
	s_waitcnt vmcnt(0)
	v_pk_mul_f32 v[4:5], v[8:9], v[4:5]
	s_nop 0
	v_cvt_pk_fp8_f32 v12, v4, v5
	v_pk_mul_f32 v[6:7], v[10:11], v[6:7]
	v_cvt_pk_bf16_f32 v4, v4, v5
	s_nop 0
	v_cvt_pk_fp8_f32 v12, v6, v7 op_sel:[0,0,1]
	v_cvt_pk_bf16_f32 v5, v6, v7
	global_store_dwordx2 v[60:61], v[4:5], off offset:3072
	global_store_dword v[62:63], v12, off offset:1536
	global_load_dwordx4 v[4:7], v[26:27], off
	s_waitcnt vmcnt(0)
	v_pk_mul_f32 v[0:1], v[4:5], v[0:1]
	s_nop 0
	v_cvt_pk_fp8_f32 v65, v0, v1
	v_cvt_pk_bf16_f32 v0, v0, v1
	v_pk_mul_f32 v[2:3], v[64:65], v[2:3] op_sel_hi:[0,1]
	v_pk_mul_f32 v[2:3], v[6:7], v[2:3]
	s_nop 0
	v_cvt_pk_fp8_f32 v65, v2, v3 op_sel:[0,0,1]
	v_cvt_pk_bf16_f32 v1, v2, v3
	global_store_dwordx2 v[60:61], v[0:1], off offset:3584
	global_store_dword v[62:63], v65, off offset:1792
	s_cbranch_scc0 .LBB0_46
